# GU L1 K-loop: LDS-DMA issue rebalanced 2+6 -> 4+4 per load phase (A x0 half-tile staged one phase later), waits 8/6
# speedup vs baseline: 1.0221x; 1.0041x over previous
; #define PG8_STAGE(bufoff, gbase, voff) do { _Pragma("unroll") for (int _i = 0; _i < 2; ++_i) \
;         __builtin_amdgcn_global_load_lds((const unsigned*)((const char*)(gbase) + (voff)[_i]), (LAS unsigned*)(lds + (bufoff) + ldsw + _i * 8192), 16, 0, 0); } while (0)
; #define PG8_WAIT_V(n) asm volatile("s_waitcnt vmcnt(" #n ")" ::: "memory")
; #define PG8_BAR __builtin_amdgcn_s_barrier()
;     ...
;     PG8_STAGE(PG8_SB(0, 0), cB, voffB); PG8_STAGE(PG8_SB(0, 1), cB + hstep, voffB); PG8_STAGE(PG8_SA(0, 0), cA, voffA[0]); PG8_STAGE(PG8_SA(0, 1), cA, voffA[1]);
;     if (wr == 1) PG8_BAR;
;     PG8_WAIT_V(2); PG8_BAR;
;     PG8_STAGE(PG8_SB(1, 0), cB + kstepB, voffB); PG8_STAGE(PG8_SA(1, 0), cA + kstepA, voffA[0]); PG8_STAGE(PG8_SB(1, 1), cB + hstep + kstepB, voffB);
;     PG8_WAIT_V(6); PG8_BAR;
.LBB0_2329:
	s_lshl_b32 s7, s7, 3
	s_lshl_b32 s39, s6, 6
	s_lshl_b32 s6, s0, 5
	s_sub_i32 s1, s1, s7
	s_and_b32 s40, s6, 0x60
	s_add_u32 s6, s2, 0x4000
	s_addc_u32 s7, s3, 0
	s_add_i32 m0, s17, 0x18000
	v_lshl_add_u64 v[4:5], s[6:7], 0, v[132:133]
	s_waitcnt vmcnt(2)
	s_barrier
	global_load_lds_dwordx4 v[4:5], off
	s_add_i32 m0, s17, 0x1a000
	v_lshl_add_u64 v[4:5], s[6:7], 0, v[134:135]
	s_add_u32 s6, s90, 0x4213680
	s_addc_u32 s7, s91, 0
	s_add_i32 s41, s17, 0x8000
	s_add_i32 s42, s17, 0xa000
	global_load_lds_dwordx4 v[4:5], off
	v_lshl_add_u64 v[234:235], s[6:7], 0, v[136:137]
	v_lshl_add_u64 v[4:5], s[6:7], 0, v[136:137]
	s_mov_b32 m0, s41
	s_add_u32 s10, s2, 0x44000
	global_load_lds_dwordx4 v[4:5], off
	v_lshl_add_u64 v[232:233], s[6:7], 0, v[2:3]
	v_lshl_add_u64 v[2:3], s[6:7], 0, v[2:3]
	s_mov_b32 m0, s42
	s_addc_u32 s11, s3, 0
	global_load_lds_dwordx4 v[2:3], off
	s_add_i32 m0, s17, 0x1c000
	v_lshl_add_u64 v[2:3], s[10:11], 0, v[132:133]
	global_load_lds_dwordx4 v[2:3], off
	v_lshl_add_u64 v[2:3], s[10:11], 0, v[134:135]
	s_add_i32 m0, s17, 0x1e000
	v_bfe_u32 v4, v6, 4, 2
	global_load_lds_dwordx4 v[2:3], off
	v_lshrrev_b32_e32 v2, 4, v6
	v_and_b32_e32 v3, 15, v6
	v_and_b32_e32 v6, 7, v6
	v_bitop3_b32 v2, v2, v6, 3 bitop3:0x6c
	s_cmpk_lt_u32 s8, 0x100
	v_lshlrev_b32_e32 v7, 4, v2
	v_or_b32_e32 v2, s40, v3
	s_cselect_b64 s[8:9], -1, 0
	s_lshl_b32 s0, s0, 6
	v_or_b32_e32 v5, s39, v3
	v_lshlrev_b32_e32 v9, 7, v2
	v_and_or_b32 v2, s39, 64, v3
	s_and_b32 s0, s0, 64
	s_sext_i32_i8 s52, s1
	v_lshlrev_b32_e32 v5, 7, v5
	s_waitcnt vmcnt(6)
	v_lshl_or_b32 v136, v4, 4, s0
	v_readlane_b32 s0, v250, 32
	v_lshlrev_b32_e32 v2, 6, v2
	v_or_b32_e32 v8, v5, v7
	v_readlane_b32 s1, v250, 33
	v_or_b32_e32 v4, 0x800, v2
	v_or_b32_e32 v6, 0xc00, v2
	v_bitop3_b32 v3, v5, 64, v7 bitop3:0x36
	v_or_b32_e32 v159, v9, v7
	v_lshl_add_u64 v[138:139], s[0:1], 0, v[136:137]
	v_bitop3_b32 v160, v9, 64, v7 bitop3:0x36
	s_add_i32 s43, 0, 0x10000
	s_add_i32 s44, 0, 0x10800
	s_add_i32 s45, 0, 0x14000
	s_add_i32 s46, 0, 0x14800
	v_add_u32_e32 v161, 0, v8
	v_add_u32_e32 v162, 0, v3
	s_add_i32 s47, 0, 0x18800
	s_add_i32 s48, 0, 0x1c800
	s_mov_b64 s[10:11], 0x80
	v_lshlrev_b32_e32 v140, 1, v2
	v_lshlrev_b32_e32 v142, 1, v4
	v_lshlrev_b32_e32 v144, 1, v6
	v_mov_b32_e32 v163, 0xc60000
	s_barrier
	s_branch .LBB0_2332

; #define PG8_STAGE(bufoff, gbase, voff) do { _Pragma("unroll") for (int _i = 0; _i < 2; ++_i) \
;         __builtin_amdgcn_global_load_lds((const unsigned*)((const char*)(gbase) + (voff)[_i]), (LAS unsigned*)(lds + (bufoff) + ldsw + _i * 8192), 16, 0, 0); } while (0)
; #define PG8_LDA(dst, b, h) do { _Pragma("unroll") for (int m = 0; m < 4; ++m) _Pragma("unroll") for (int k = 0; k < 2; ++k) dst[m][k] = *(const LAS bf16x8*)(lds + PG8_SA(b, h) + ((aoff ^ (k * 64)) + m * 2048)); } while (0)
; #define PG8_LDB(dst, b, h) do { _Pragma("unroll") for (int n = 0; n < 2; ++n) _Pragma("unroll") for (int k = 0; k < 2; ++k) dst[n][k] = *(const LAS bf16x8*)(lds + PG8_SB(b, h) + ((boff ^ (k * 64)) + n * 2048)); } while (0)
; #define PG8_WAIT_V(n) asm volatile("s_waitcnt vmcnt(" #n ")" ::: "memory")
; #define PG8_WAIT_L(n) asm volatile("s_waitcnt lgkmcnt(" #n ")" ::: "memory")
;     ...
;             const bool last = (t == nt - 2);
;             const char* a1 = cA + (size_t)(t + 1) * kstepA;
;             const char* a2 = last ? nA : cA + (size_t)(t + 2) * kstepA; const char* b2 = last ? nB : cB + (size_t)(t + 2) * kstepB;
;             const char* a3 = a2 + kstepA; const char* b3 = b2 + kstepB;
;             unsigned vs[2][2];
;             if constexpr (GATHER) {
;                 if (last && has_next) {
; #pragma unroll
;                     for (int hh = 0; hh < 2; ++hh)
; #pragma unroll
;                         for (int i = 0; i < 2; ++i) voffN[hh][i] = (unsigned)idxl[(ui + 1) * 256 + hh * HALF + sR[i]] * (unsigned)(K * 2) + (unsigned)sC[i] * 2u;
;                 }
; #pragma unroll
;                 for (int hh = 0; hh < 2; ++hh)
; #pragma unroll
;                     for (int i = 0; i < 2; ++i) vs[hh][i] = last ? voffN[hh][i] : voffA[hh][i];
;             } else {
; #pragma unroll
;                 for (int hh = 0; hh < 2; ++hh)
; #pragma unroll
;                     for (int i = 0; i < 2; ++i) vs[hh][i] = voffA[hh][i];
;             }
;             PG8_LDB(B0, 0, 0); PG8_LDB(B1, 0, 1); PG8_SCHED; PG8_LDA(At, 0, 0); PG8_STAGE(PG8_SA(1, 1), a1, voffA[1]);
;             PG8_WAIT_V(8); PG8_WAIT_L(0); PG8_BAR; if (do0) { PG8_MMA(0, 0, At, B0); PG8_MMA(0, 1, At, B1); } PG8_BAR; PG8_SCHED;
;             PG8_LDA(At, 0, 1); PG8_STAGE(PG8_SB(0, 0), b2, voffB); PG8_STAGE(PG8_SB(0, 1), b2 + hstep, voffB); PG8_STAGE(PG8_SA(0, 0), a2, vs[0]);
.LBB0_2337:
	v_add_u32_e32 v136, s43, v159
	v_add_u32_e32 v145, s43, v160
	ds_read_b128 v[166:169], v136
	ds_read_b128 v[170:173], v145
	v_add_u32_e32 v136, s44, v159
	s_add_u32 s22, s90, s20
	v_add_u32_e32 v145, s44, v160
	ds_read_b128 v[174:177], v136
	ds_read_b128 v[178:181], v145
	v_add_u32_e32 v136, s45, v159
	s_addc_u32 s23, s91, s21
	v_add_u32_e32 v145, s45, v160
	ds_read_b128 v[182:185], v136
	ds_read_b128 v[186:189], v145
	v_add_u32_e32 v136, s46, v159
	s_add_u32 s24, s22, 0x4213700
	v_add_u32_e32 v145, s46, v160
	ds_read_b128 v[190:193], v136
	ds_read_b128 v[194:197], v145
	s_addc_u32 s25, s23, 0
	s_and_b64 s[22:23], s[2:3], exec
	s_cselect_b32 s22, s14, s13
	s_cselect_b32 s27, s83, s25
	s_cselect_b32 s26, s82, s24
	s_cselect_b32 s23, s15, s53
	s_add_u32 s24, s22, 0x4000
	s_addc_u32 s25, s23, 0
	s_mov_b32 m0, s41
	s_nop 0
	global_load_lds_dwordx4 v[234:235], off
	s_mov_b32 m0, s42
	s_nop 0
	global_load_lds_dwordx4 v[232:233], off
	v_cndmask_b32_e64 v136, v152, v146, s[2:3]
	v_cndmask_b32_e64 v232, v153, v147, s[2:3]
	v_cndmask_b32_e64 v145, v148, v164, s[2:3]
	v_cndmask_b32_e64 v149, v150, v165, s[2:3]
	v_lshl_add_u64 v[234:235], v[156:157], 0, s[20:21]
	s_add_i32 m0, s17, 0xc000
	ds_read_b128 v[200:203], v161
	ds_read_b128 v[204:207], v161 offset:2048
	ds_read_b128 v[208:211], v162
	ds_read_b128 v[212:215], v162 offset:2048
	ds_read_b128 v[216:219], v161 offset:4096
	ds_read_b128 v[220:223], v161 offset:6144
	ds_read_b128 v[224:227], v162 offset:4096
	ds_read_b128 v[228:231], v162 offset:6144
	global_load_lds_dwordx4 v[234:235], off
	v_lshl_add_u64 v[234:235], v[154:155], 0, s[20:21]
	s_add_i32 m0, s17, 0xe000
	s_nop 0
	global_load_lds_dwordx4 v[234:235], off
	s_waitcnt vmcnt(8)
	s_waitcnt lgkmcnt(0)
	s_barrier
	s_setprio 1
	s_waitcnt lgkmcnt(0)
	v_mfma_f32_16x16x32_bf16 v[126:129], v[166:169], v[200:203], v[126:129]
	v_mfma_f32_16x16x32_bf16 v[122:125], v[174:177], v[200:203], v[122:125]
	v_mfma_f32_16x16x32_bf16 v[110:113], v[166:169], v[204:207], v[110:113]
	v_mfma_f32_16x16x32_bf16 v[106:109], v[174:177], v[204:207], v[106:109]
	v_mfma_f32_16x16x32_bf16 v[94:97], v[166:169], v[216:219], v[94:97]
	v_mfma_f32_16x16x32_bf16 v[90:93], v[174:177], v[216:219], v[90:93]
	v_mfma_f32_16x16x32_bf16 v[78:81], v[166:169], v[220:223], v[78:81]
	v_mfma_f32_16x16x32_bf16 v[74:77], v[174:177], v[220:223], v[74:77]
	v_mfma_f32_16x16x32_bf16 v[126:129], v[170:173], v[208:211], v[126:129]
	v_mfma_f32_16x16x32_bf16 v[122:125], v[178:181], v[208:211], v[122:125]
	v_mfma_f32_16x16x32_bf16 v[110:113], v[170:173], v[212:215], v[110:113]
	v_mfma_f32_16x16x32_bf16 v[106:109], v[178:181], v[212:215], v[106:109]
	v_mfma_f32_16x16x32_bf16 v[94:97], v[170:173], v[224:227], v[94:97]
	v_mfma_f32_16x16x32_bf16 v[90:93], v[178:181], v[224:227], v[90:93]
	v_mfma_f32_16x16x32_bf16 v[78:81], v[170:173], v[228:231], v[78:81]
	v_mfma_f32_16x16x32_bf16 v[74:77], v[178:181], v[228:231], v[74:77]
	s_setprio 0
	s_setprio 1
	v_mfma_f32_16x16x32_bf16 v[118:121], v[182:185], v[200:203], v[118:121]
	v_mfma_f32_16x16x32_bf16 v[114:117], v[190:193], v[200:203], v[114:117]
	v_mfma_f32_16x16x32_bf16 v[102:105], v[182:185], v[204:207], v[102:105]
	v_mfma_f32_16x16x32_bf16 v[98:101], v[190:193], v[204:207], v[98:101]
	v_mfma_f32_16x16x32_bf16 v[86:89], v[182:185], v[216:219], v[86:89]
	v_mfma_f32_16x16x32_bf16 v[82:85], v[190:193], v[216:219], v[82:85]
	v_mfma_f32_16x16x32_bf16 v[70:73], v[182:185], v[220:223], v[70:73]
	v_mfma_f32_16x16x32_bf16 v[66:69], v[190:193], v[220:223], v[66:69]
	v_mfma_f32_16x16x32_bf16 v[118:121], v[186:189], v[208:211], v[118:121]
	v_mfma_f32_16x16x32_bf16 v[114:117], v[194:197], v[208:211], v[114:117]
	v_mfma_f32_16x16x32_bf16 v[102:105], v[186:189], v[212:215], v[102:105]
	v_mfma_f32_16x16x32_bf16 v[98:101], v[194:197], v[212:215], v[98:101]
	v_mfma_f32_16x16x32_bf16 v[86:89], v[186:189], v[224:227], v[86:89]
	v_mfma_f32_16x16x32_bf16 v[82:85], v[194:197], v[224:227], v[82:85]
	v_mfma_f32_16x16x32_bf16 v[70:73], v[186:189], v[228:231], v[70:73]
	v_mfma_f32_16x16x32_bf16 v[66:69], v[194:197], v[228:231], v[66:69]
	s_setprio 0
	s_barrier
	s_add_i32 s2, s43, s34
	v_lshl_add_u64 v[234:235], s[22:23], 0, v[132:133]
	s_mov_b32 m0, s2
	ds_read_b128 v[200:203], v161 offset:16384
	ds_read_b128 v[204:207], v161 offset:18432
	ds_read_b128 v[208:211], v162 offset:16384
	ds_read_b128 v[212:215], v162 offset:18432
	ds_read_b128 v[216:219], v161 offset:20480
	ds_read_b128 v[220:223], v161 offset:22528
	ds_read_b128 v[224:227], v162 offset:20480
	ds_read_b128 v[228:231], v162 offset:22528
	global_load_lds_dwordx4 v[234:235], off
	s_add_i32 m0, s2, 0x2000
	s_add_u32 s2, s22, 0x40000
	v_lshl_add_u64 v[234:235], s[22:23], 0, v[134:135]
	s_addc_u32 s3, s23, 0
	s_add_i32 s55, s45, s34
	global_load_lds_dwordx4 v[234:235], off
	v_lshl_add_u64 v[234:235], s[2:3], 0, v[132:133]
	s_mov_b32 m0, s55
	v_mov_b32_e32 v233, v137
	global_load_lds_dwordx4 v[234:235], off
	v_lshl_add_u64 v[234:235], s[2:3], 0, v[134:135]
	s_add_i32 m0, s55, 0x2000
	s_nop 0
	global_load_lds_dwordx4 v[234:235], off
	v_lshl_add_u64 v[234:235], s[26:27], 0, v[136:137]
	s_waitcnt vmcnt(6)
	s_waitcnt lgkmcnt(0)
	v_lshl_add_u64 v[232:233], s[26:27], 0, v[232:233]
	s_barrier
; #define PG8_STAGE(bufoff, gbase, voff) do { _Pragma("unroll") for (int _i = 0; _i < 2; ++_i) \
;         __builtin_amdgcn_global_load_lds((const unsigned*)((const char*)(gbase) + (voff)[_i]), (LAS unsigned*)(lds + (bufoff) + ldsw + _i * 8192), 16, 0, 0); } while (0)
; #define PG8_LDA(dst, b, h) do { _Pragma("unroll") for (int m = 0; m < 4; ++m) _Pragma("unroll") for (int k = 0; k < 2; ++k) dst[m][k] = *(const LAS bf16x8*)(lds + PG8_SA(b, h) + ((aoff ^ (k * 64)) + m * 2048)); } while (0)
; #define PG8_LDB(dst, b, h) do { _Pragma("unroll") for (int n = 0; n < 2; ++n) _Pragma("unroll") for (int k = 0; k < 2; ++k) dst[n][k] = *(const LAS bf16x8*)(lds + PG8_SB(b, h) + ((boff ^ (k * 64)) + n * 2048)); } while (0)
; #define PG8_MMA(ai, bj, At, Bt) do { __builtin_amdgcn_s_setprio(1); _Pragma("unroll") for (int m = 0; m < 4; ++m) _Pragma("unroll") for (int n = 0; n < 2; ++n) _Pragma("unroll") for (int k = 0; k < 2; ++k) \
;         acc[ai][bj][m][n] = __builtin_amdgcn_mfma_f32_16x16x32_bf16(Bt[n][k], At[m][k], acc[ai][bj][m][n], 0, 0, 0); __builtin_amdgcn_s_setprio(0); } while (0)
; #define PG8_WAIT_V(n) asm volatile("s_waitcnt vmcnt(" #n ")" ::: "memory")
; #define PG8_WAIT_L(n) asm volatile("s_waitcnt lgkmcnt(" #n ")" ::: "memory")
; #define PG8_BAR __builtin_amdgcn_s_barrier()
; #define PG8_SCHED __builtin_amdgcn_sched_barrier(0)
;     ...
;             PG8_WAIT_V(8); PG8_WAIT_L(0); PG8_BAR; if (do1) { PG8_MMA(1, 0, At, B0); PG8_MMA(1, 1, At, B1); } PG8_BAR; PG8_SCHED;
;             PG8_LDB(B0, 1, 0); PG8_LDB(B1, 1, 1); PG8_SCHED; PG8_LDA(At, 1, 0); PG8_STAGE(PG8_SA(0, 1), a2, vs[1]);
;             PG8_WAIT_V(8); PG8_WAIT_L(0); PG8_BAR; if (do0) { PG8_MMA(0, 0, At, B0); PG8_MMA(0, 1, At, B1); } PG8_BAR; PG8_SCHED;
;             PG8_LDA(At, 1, 1); PG8_STAGE(PG8_SB(1, 0), b3, voffB); PG8_STAGE(PG8_SB(1, 1), b3 + hstep, voffB); PG8_STAGE(PG8_SA(1, 0), a3, vs[0]);
	s_setprio 1
	s_waitcnt lgkmcnt(0)
	v_mfma_f32_16x16x32_bf16 v[62:65], v[166:169], v[200:203], v[62:65]
	v_mfma_f32_16x16x32_bf16 v[58:61], v[174:177], v[200:203], v[58:61]
	v_mfma_f32_16x16x32_bf16 v[46:49], v[166:169], v[204:207], v[46:49]
	v_mfma_f32_16x16x32_bf16 v[42:45], v[174:177], v[204:207], v[42:45]
	v_mfma_f32_16x16x32_bf16 v[30:33], v[166:169], v[216:219], v[30:33]
	v_mfma_f32_16x16x32_bf16 v[26:29], v[174:177], v[216:219], v[26:29]
	v_mfma_f32_16x16x32_bf16 v[14:17], v[166:169], v[220:223], v[14:17]
	v_mfma_f32_16x16x32_bf16 v[10:13], v[174:177], v[220:223], v[10:13]
	v_mfma_f32_16x16x32_bf16 v[62:65], v[170:173], v[208:211], v[62:65]
	v_mfma_f32_16x16x32_bf16 v[58:61], v[178:181], v[208:211], v[58:61]
	v_mfma_f32_16x16x32_bf16 v[46:49], v[170:173], v[212:215], v[46:49]
	v_mfma_f32_16x16x32_bf16 v[42:45], v[178:181], v[212:215], v[42:45]
	v_mfma_f32_16x16x32_bf16 v[30:33], v[170:173], v[224:227], v[30:33]
	v_mfma_f32_16x16x32_bf16 v[26:29], v[178:181], v[224:227], v[26:29]
	v_mfma_f32_16x16x32_bf16 v[14:17], v[170:173], v[228:231], v[14:17]
	v_mfma_f32_16x16x32_bf16 v[10:13], v[178:181], v[228:231], v[10:13]
	s_setprio 0
	s_setprio 1
	v_mfma_f32_16x16x32_bf16 v[54:57], v[182:185], v[200:203], v[54:57]
	v_mfma_f32_16x16x32_bf16 v[50:53], v[190:193], v[200:203], v[50:53]
	v_mfma_f32_16x16x32_bf16 v[38:41], v[182:185], v[204:207], v[38:41]
	v_mfma_f32_16x16x32_bf16 v[34:37], v[190:193], v[204:207], v[34:37]
	v_mfma_f32_16x16x32_bf16 v[22:25], v[182:185], v[216:219], v[22:25]
	v_mfma_f32_16x16x32_bf16 v[18:21], v[190:193], v[216:219], v[18:21]
	v_mfma_f32_16x16x32_bf16 v[6:9], v[182:185], v[220:223], v[6:9]
	v_mfma_f32_16x16x32_bf16 v[2:5], v[190:193], v[220:223], v[2:5]
	v_mfma_f32_16x16x32_bf16 v[54:57], v[186:189], v[208:211], v[54:57]
	v_mfma_f32_16x16x32_bf16 v[50:53], v[194:197], v[208:211], v[50:53]
	v_mfma_f32_16x16x32_bf16 v[38:41], v[186:189], v[212:215], v[38:41]
	v_mfma_f32_16x16x32_bf16 v[34:37], v[194:197], v[212:215], v[34:37]
	v_mfma_f32_16x16x32_bf16 v[22:25], v[186:189], v[224:227], v[22:25]
	v_mfma_f32_16x16x32_bf16 v[18:21], v[194:197], v[224:227], v[18:21]
	v_mfma_f32_16x16x32_bf16 v[6:9], v[186:189], v[228:231], v[6:9]
	v_mfma_f32_16x16x32_bf16 v[2:5], v[194:197], v[228:231], v[2:5]
	s_setprio 0
	s_barrier
	s_add_i32 s2, 0, 0x18000
	v_add_u32_e32 v136, s2, v159
	v_add_u32_e32 v151, s2, v160
	ds_read_b128 v[166:169], v136
	ds_read_b128 v[170:173], v151
	v_add_u32_e32 v136, s47, v159
	s_add_i32 s55, 0, 0x1c000
	v_add_u32_e32 v151, s47, v160
	ds_read_b128 v[174:177], v136
	ds_read_b128 v[178:181], v151
	v_add_u32_e32 v136, s55, v159
	v_add_u32_e32 v151, s55, v160
	ds_read_b128 v[182:185], v136
	ds_read_b128 v[186:189], v151
	v_add_u32_e32 v136, s48, v159
	v_add_u32_e32 v151, s48, v160
	ds_read_b128 v[190:193], v136
	ds_read_b128 v[194:197], v151
	s_mov_b32 m0, s17
	s_nop 0
	global_load_lds_dwordx4 v[234:235], off
	s_mov_b32 m0, s35
	s_nop 0
	global_load_lds_dwordx4 v[232:233], off
	s_mov_b32 m0, s36
	ds_read_b128 v[200:203], v161 offset:32768
	ds_read_b128 v[204:207], v161 offset:34816
	ds_read_b128 v[208:211], v162 offset:32768
	ds_read_b128 v[212:215], v162 offset:34816
	ds_read_b128 v[216:219], v161 offset:36864
	ds_read_b128 v[220:223], v161 offset:38912
	ds_read_b128 v[224:227], v162 offset:36864
	ds_read_b128 v[228:231], v162 offset:38912
	global_load_lds_dwordx4 v145, s[26:27]
	s_mov_b32 m0, s37
	s_nop 0
	global_load_lds_dwordx4 v149, s[26:27]
	s_waitcnt vmcnt(8)
	s_waitcnt lgkmcnt(0)
	s_barrier
	s_setprio 1
	s_waitcnt lgkmcnt(0)
	v_mfma_f32_16x16x32_bf16 v[126:129], v[166:169], v[200:203], v[126:129]
	v_mfma_f32_16x16x32_bf16 v[122:125], v[174:177], v[200:203], v[122:125]
	v_mfma_f32_16x16x32_bf16 v[110:113], v[166:169], v[204:207], v[110:113]
	v_mfma_f32_16x16x32_bf16 v[106:109], v[174:177], v[204:207], v[106:109]
	v_mfma_f32_16x16x32_bf16 v[94:97], v[166:169], v[216:219], v[94:97]
	v_mfma_f32_16x16x32_bf16 v[90:93], v[174:177], v[216:219], v[90:93]
	v_mfma_f32_16x16x32_bf16 v[78:81], v[166:169], v[220:223], v[78:81]
	v_mfma_f32_16x16x32_bf16 v[74:77], v[174:177], v[220:223], v[74:77]
	v_mfma_f32_16x16x32_bf16 v[126:129], v[170:173], v[208:211], v[126:129]
	v_mfma_f32_16x16x32_bf16 v[122:125], v[178:181], v[208:211], v[122:125]
	v_mfma_f32_16x16x32_bf16 v[110:113], v[170:173], v[212:215], v[110:113]
	v_mfma_f32_16x16x32_bf16 v[106:109], v[178:181], v[212:215], v[106:109]
	v_mfma_f32_16x16x32_bf16 v[94:97], v[170:173], v[224:227], v[94:97]
	v_mfma_f32_16x16x32_bf16 v[90:93], v[178:181], v[224:227], v[90:93]
	v_mfma_f32_16x16x32_bf16 v[78:81], v[170:173], v[228:231], v[78:81]
	v_mfma_f32_16x16x32_bf16 v[74:77], v[178:181], v[228:231], v[74:77]
	s_setprio 0
	s_setprio 1
	v_mfma_f32_16x16x32_bf16 v[118:121], v[182:185], v[200:203], v[118:121]
	v_mfma_f32_16x16x32_bf16 v[114:117], v[190:193], v[200:203], v[114:117]
	v_mfma_f32_16x16x32_bf16 v[102:105], v[182:185], v[204:207], v[102:105]
	v_mfma_f32_16x16x32_bf16 v[98:101], v[190:193], v[204:207], v[98:101]
	v_mfma_f32_16x16x32_bf16 v[86:89], v[182:185], v[216:219], v[86:89]
	v_mfma_f32_16x16x32_bf16 v[82:85], v[190:193], v[216:219], v[82:85]
	v_mfma_f32_16x16x32_bf16 v[70:73], v[182:185], v[220:223], v[70:73]
	v_mfma_f32_16x16x32_bf16 v[66:69], v[190:193], v[220:223], v[66:69]
	v_mfma_f32_16x16x32_bf16 v[118:121], v[186:189], v[208:211], v[118:121]
	v_mfma_f32_16x16x32_bf16 v[114:117], v[194:197], v[208:211], v[114:117]
	v_mfma_f32_16x16x32_bf16 v[102:105], v[186:189], v[212:215], v[102:105]
	v_mfma_f32_16x16x32_bf16 v[98:101], v[194:197], v[212:215], v[98:101]
	v_mfma_f32_16x16x32_bf16 v[86:89], v[186:189], v[224:227], v[86:89]
	v_mfma_f32_16x16x32_bf16 v[82:85], v[194:197], v[224:227], v[82:85]
	v_mfma_f32_16x16x32_bf16 v[70:73], v[186:189], v[228:231], v[70:73]
	v_mfma_f32_16x16x32_bf16 v[66:69], v[194:197], v[228:231], v[66:69]
	s_setprio 0
	s_barrier
; #define PG8_STAGE(bufoff, gbase, voff) do { _Pragma("unroll") for (int _i = 0; _i < 2; ++_i) \
;         __builtin_amdgcn_global_load_lds((const unsigned*)((const char*)(gbase) + (voff)[_i]), (LAS unsigned*)(lds + (bufoff) + ldsw + _i * 8192), 16, 0, 0); } while (0)
; #define PG8_LDA(dst, b, h) do { _Pragma("unroll") for (int m = 0; m < 4; ++m) _Pragma("unroll") for (int k = 0; k < 2; ++k) dst[m][k] = *(const LAS bf16x8*)(lds + PG8_SA(b, h) + ((aoff ^ (k * 64)) + m * 2048)); } while (0)
; #define PG8_MMA(ai, bj, At, Bt) do { __builtin_amdgcn_s_setprio(1); _Pragma("unroll") for (int m = 0; m < 4; ++m) _Pragma("unroll") for (int n = 0; n < 2; ++n) _Pragma("unroll") for (int k = 0; k < 2; ++k) \
;         acc[ai][bj][m][n] = __builtin_amdgcn_mfma_f32_16x16x32_bf16(Bt[n][k], At[m][k], acc[ai][bj][m][n], 0, 0, 0); __builtin_amdgcn_s_setprio(0); } while (0)
; #define PG8_WAIT_V(n) asm volatile("s_waitcnt vmcnt(" #n ")" ::: "memory")
; #define PG8_WAIT_L(n) asm volatile("s_waitcnt lgkmcnt(" #n ")" ::: "memory")
; #define PG8_BAR __builtin_amdgcn_s_barrier()
; #define PG8_SCHED __builtin_amdgcn_sched_barrier(0)
;     ...
;             PG8_LDA(At, 1, 1); PG8_STAGE(PG8_SB(1, 0), b3, voffB); PG8_STAGE(PG8_SB(1, 1), b3 + hstep, voffB); PG8_STAGE(PG8_SA(1, 0), a3, vs[0]);
;             PG8_WAIT_V(8); PG8_WAIT_L(0); PG8_BAR; if (do1) { PG8_MMA(1, 0, At, B0); PG8_MMA(1, 1, At, B1); } PG8_BAR; PG8_SCHED;
;         }
	s_add_i32 s2, s2, s34
	v_lshl_add_u64 v[236:237], s[24:25], 0, v[132:133]
	s_mov_b32 m0, s2
	ds_read_b128 v[200:203], v161 offset:49152
	ds_read_b128 v[204:207], v161 offset:51200
	ds_read_b128 v[208:211], v162 offset:49152
	ds_read_b128 v[212:215], v162 offset:51200
	ds_read_b128 v[216:219], v161 offset:53248
	ds_read_b128 v[220:223], v161 offset:55296
	ds_read_b128 v[224:227], v162 offset:53248
	ds_read_b128 v[228:231], v162 offset:55296
	global_load_lds_dwordx4 v[236:237], off
	s_add_i32 m0, s2, 0x2000
	s_add_u32 s2, s22, 0x44000
	v_lshl_add_u64 v[236:237], s[24:25], 0, v[134:135]
	s_addc_u32 s3, s23, 0
	s_add_i32 s22, s55, s34
	global_load_lds_dwordx4 v[236:237], off
	v_lshl_add_u64 v[236:237], s[2:3], 0, v[132:133]
	s_mov_b32 m0, s22
	v_lshl_add_u64 v[234:235], v[234:235], 0, s[10:11]
	global_load_lds_dwordx4 v[236:237], off
	v_lshl_add_u64 v[236:237], s[2:3], 0, v[134:135]
	s_add_i32 m0, s22, 0x2000
	v_lshl_add_u64 v[232:233], v[232:233], 0, s[10:11]
	global_load_lds_dwordx4 v[236:237], off
	s_waitcnt vmcnt(6)
	s_waitcnt lgkmcnt(0)
	s_barrier
	s_setprio 1
	s_waitcnt lgkmcnt(0)
	v_mfma_f32_16x16x32_bf16 v[62:65], v[166:169], v[200:203], v[62:65]
	v_mfma_f32_16x16x32_bf16 v[58:61], v[174:177], v[200:203], v[58:61]
	v_mfma_f32_16x16x32_bf16 v[46:49], v[166:169], v[204:207], v[46:49]
	v_mfma_f32_16x16x32_bf16 v[42:45], v[174:177], v[204:207], v[42:45]
	v_mfma_f32_16x16x32_bf16 v[30:33], v[166:169], v[216:219], v[30:33]
	v_mfma_f32_16x16x32_bf16 v[26:29], v[174:177], v[216:219], v[26:29]
	v_mfma_f32_16x16x32_bf16 v[14:17], v[166:169], v[220:223], v[14:17]
	v_mfma_f32_16x16x32_bf16 v[10:13], v[174:177], v[220:223], v[10:13]
	v_mfma_f32_16x16x32_bf16 v[62:65], v[170:173], v[208:211], v[62:65]
	v_mfma_f32_16x16x32_bf16 v[58:61], v[178:181], v[208:211], v[58:61]
	v_mfma_f32_16x16x32_bf16 v[46:49], v[170:173], v[212:215], v[46:49]
	v_mfma_f32_16x16x32_bf16 v[42:45], v[178:181], v[212:215], v[42:45]
	v_mfma_f32_16x16x32_bf16 v[30:33], v[170:173], v[224:227], v[30:33]
	v_mfma_f32_16x16x32_bf16 v[26:29], v[178:181], v[224:227], v[26:29]
	v_mfma_f32_16x16x32_bf16 v[14:17], v[170:173], v[228:231], v[14:17]
	v_mfma_f32_16x16x32_bf16 v[10:13], v[178:181], v[228:231], v[10:13]
	s_setprio 0
	s_setprio 1
	v_mfma_f32_16x16x32_bf16 v[54:57], v[182:185], v[200:203], v[54:57]
	v_mfma_f32_16x16x32_bf16 v[50:53], v[190:193], v[200:203], v[50:53]
	v_mfma_f32_16x16x32_bf16 v[38:41], v[182:185], v[204:207], v[38:41]
	v_mfma_f32_16x16x32_bf16 v[34:37], v[190:193], v[204:207], v[34:37]
	v_mfma_f32_16x16x32_bf16 v[22:25], v[182:185], v[216:219], v[22:25]
	v_mfma_f32_16x16x32_bf16 v[18:21], v[190:193], v[216:219], v[18:21]
	v_mfma_f32_16x16x32_bf16 v[6:9], v[182:185], v[220:223], v[6:9]
	v_mfma_f32_16x16x32_bf16 v[2:5], v[190:193], v[220:223], v[2:5]
	v_mfma_f32_16x16x32_bf16 v[54:57], v[186:189], v[208:211], v[54:57]
	v_mfma_f32_16x16x32_bf16 v[50:53], v[194:197], v[208:211], v[50:53]
	v_mfma_f32_16x16x32_bf16 v[38:41], v[186:189], v[212:215], v[38:41]
	v_mfma_f32_16x16x32_bf16 v[34:37], v[194:197], v[212:215], v[34:37]
	v_mfma_f32_16x16x32_bf16 v[22:25], v[186:189], v[224:227], v[22:25]
	v_mfma_f32_16x16x32_bf16 v[18:21], v[194:197], v[224:227], v[18:21]
	v_mfma_f32_16x16x32_bf16 v[6:9], v[186:189], v[228:231], v[6:9]
	v_mfma_f32_16x16x32_bf16 v[2:5], v[194:197], v[228:231], v[2:5]
	s_setprio 0
	s_barrier
	s_add_i32 s54, s54, 2
	s_add_u32 s13, s13, 0x8000
	s_addc_u32 s53, s53, 0
	s_add_u32 s20, s20, 0x100
	s_addc_u32 s21, s21, 0
	s_cmp_gt_u32 s54, 13
	s_cbranch_scc1 .LBB0_2340
